# GEMM sub-phases: MFMAs issued in snake order so that only one of the two operand fragments changes between consecutive MFMAs
# baseline (speedup 1.0000x reference)
.LBB0_247:
	s_add_u32 s50, s48, 0x80
	s_addc_u32 s51, s49, 0
	s_add_i32 s74, 0, 0x10000
	v_add_u32_e32 v220, s74, v147
	v_add_u32_e32 v221, s74, v148
	ds_read_b128 v[222:225], v220
	ds_read_b128 v[230:233], v220 offset:2048
	ds_read_b128 v[226:229], v221
	ds_read_b128 v[234:237], v221 offset:2048
	s_cmp_eq_u32 s73, 12
	s_cselect_b32 s53, s5, s51
	s_cselect_b32 s52, s43, s50
	s_cselect_b32 s51, s8, s72
	s_cselect_b32 s50, s9, s67
	s_add_i32 s75, s31, s55
	v_lshl_add_u64 v[142:143], s[48:49], 0, v[140:141]
	s_mov_b32 m0, s75
	ds_read_b128 v[168:171], v150
	ds_read_b128 v[182:185], v150 offset:2048
	ds_read_b128 v[172:175], v151
	ds_read_b128 v[186:189], v151 offset:2048
	ds_read_b128 v[190:193], v150 offset:4096
	ds_read_b128 v[198:201], v150 offset:6144
	ds_read_b128 v[194:197], v151 offset:4096
	ds_read_b128 v[202:205], v151 offset:6144
	global_load_lds_dwordx4 v[142:143], off
	v_lshl_add_u64 v[142:143], s[48:49], 0, v[138:139]
	s_add_i32 m0, s75, 0x2000
	s_nop 0
	global_load_lds_dwordx4 v[142:143], off
	s_waitcnt vmcnt(6)
	s_waitcnt lgkmcnt(0)
	s_barrier
	s_setprio 1
	s_waitcnt lgkmcnt(0)
	v_mfma_f32_16x16x128_f8f6f4 v[128:131], v[222:229], v[168:175], v[128:131]
	v_mfma_f32_16x16x128_f8f6f4 v[124:127], v[230:237], v[168:175], v[124:127]
	v_mfma_f32_16x16x128_f8f6f4 v[112:115], v[230:237], v[182:189], v[112:115]
	v_mfma_f32_16x16x128_f8f6f4 v[120:123], v[222:229], v[182:189], v[120:123]
	v_mfma_f32_16x16x128_f8f6f4 v[104:107], v[222:229], v[190:197], v[104:107]
	v_mfma_f32_16x16x128_f8f6f4 v[96:99], v[230:237], v[190:197], v[96:99]
	v_mfma_f32_16x16x128_f8f6f4 v[80:83], v[230:237], v[198:205], v[80:83]
	v_mfma_f32_16x16x128_f8f6f4 v[88:91], v[222:229], v[198:205], v[88:91]
	s_setprio 0
	s_barrier
	s_add_i32 s75, 0, 0x14000
	v_add_u32_e32 v142, s75, v147
	v_add_u32_e32 v143, s75, v148
	s_mov_b32 m0, s56
	ds_read_b128 v[152:155], v142
	ds_read_b128 v[160:163], v142 offset:2048
	ds_read_b128 v[156:159], v143
	ds_read_b128 v[164:167], v143 offset:2048
	v_lshl_add_u64 v[142:143], s[50:51], 0, v[2:3]
	global_load_lds_dwordx4 v[142:143], off
	v_lshl_add_u64 v[144:145], s[50:51], 0, v[134:135]
	s_mov_b32 m0, s57
	s_nop 0
	global_load_lds_dwordx4 v[144:145], off
	s_waitcnt vmcnt(6)
	s_waitcnt lgkmcnt(0)
	s_barrier
	s_setprio 1
	s_waitcnt lgkmcnt(0)
	v_mfma_f32_16x16x128_f8f6f4 v[116:119], v[152:159], v[168:175], v[116:119]
	v_mfma_f32_16x16x128_f8f6f4 v[108:111], v[160:167], v[168:175], v[108:111]
	v_mfma_f32_16x16x128_f8f6f4 v[92:95], v[160:167], v[182:189], v[92:95]
	v_mfma_f32_16x16x128_f8f6f4 v[100:103], v[152:159], v[182:189], v[100:103]
	v_mfma_f32_16x16x128_f8f6f4 v[84:87], v[152:159], v[190:197], v[84:87]
	v_mfma_f32_16x16x128_f8f6f4 v[76:79], v[160:167], v[190:197], v[76:79]
	v_mfma_f32_16x16x128_f8f6f4 v[68:71], v[160:167], v[198:205], v[68:71]
	v_mfma_f32_16x16x128_f8f6f4 v[72:75], v[152:159], v[198:205], v[72:75]
	s_setprio 0
	s_barrier
	s_add_u32 s80, s52, 0x40000
	s_addc_u32 s81, s53, 0
	s_add_i32 s75, s75, s55
	v_lshl_add_u64 v[176:177], s[80:81], 0, v[136:137]
	s_mov_b32 m0, s75
	ds_read_b128 v[168:171], v150 offset:16384
	ds_read_b128 v[182:185], v150 offset:18432
	ds_read_b128 v[172:175], v151 offset:16384
	ds_read_b128 v[186:189], v151 offset:18432
	ds_read_b128 v[190:193], v150 offset:20480
	ds_read_b128 v[198:201], v150 offset:22528
	ds_read_b128 v[194:197], v151 offset:20480
	ds_read_b128 v[202:205], v151 offset:22528
	global_load_lds_dwordx4 v[176:177], off
	v_lshl_add_u64 v[176:177], s[80:81], 0, v[132:133]
	s_add_i32 m0, s75, 0x2000
	s_nop 0
	global_load_lds_dwordx4 v[176:177], off
	s_waitcnt vmcnt(6)
	s_waitcnt lgkmcnt(0)
	s_barrier
	s_setprio 1
	s_waitcnt lgkmcnt(0)
	v_mfma_f32_16x16x128_f8f6f4 v[52:55], v[152:159], v[168:175], v[52:55]
	v_mfma_f32_16x16x128_f8f6f4 v[44:47], v[160:167], v[168:175], v[44:47]
	v_mfma_f32_16x16x128_f8f6f4 v[28:31], v[160:167], v[182:189], v[28:31]
	v_mfma_f32_16x16x128_f8f6f4 v[36:39], v[152:159], v[182:189], v[36:39]
	v_mfma_f32_16x16x128_f8f6f4 v[20:23], v[152:159], v[190:197], v[20:23]
	v_mfma_f32_16x16x128_f8f6f4 v[12:15], v[160:167], v[190:197], v[12:15]
	v_mfma_f32_16x16x128_f8f6f4 v[4:7], v[160:167], v[198:205], v[4:7]
	v_mfma_f32_16x16x128_f8f6f4 v[8:11], v[152:159], v[198:205], v[8:11]
	s_setprio 0
	s_barrier
	s_add_u32 s80, s50, 0x40000
	s_addc_u32 s81, s51, 0
	s_mov_b32 m0, s58
	v_lshl_add_u64 v[176:177], s[80:81], 0, v[2:3]
	global_load_lds_dwordx4 v[176:177], off
	v_lshl_add_u64 v[176:177], s[80:81], 0, v[134:135]
	s_mov_b32 m0, s59
	s_nop 0
	global_load_lds_dwordx4 v[176:177], off
	s_waitcnt vmcnt(6)
	s_waitcnt lgkmcnt(0)
	s_barrier
	s_setprio 1
	s_waitcnt lgkmcnt(0)
	v_mfma_f32_16x16x128_f8f6f4 v[64:67], v[222:229], v[168:175], v[64:67]
	v_mfma_f32_16x16x128_f8f6f4 v[60:63], v[230:237], v[168:175], v[60:63]
	v_mfma_f32_16x16x128_f8f6f4 v[48:51], v[230:237], v[182:189], v[48:51]
	v_mfma_f32_16x16x128_f8f6f4 v[56:59], v[222:229], v[182:189], v[56:59]
	v_mfma_f32_16x16x128_f8f6f4 v[40:43], v[222:229], v[190:197], v[40:43]
	v_mfma_f32_16x16x128_f8f6f4 v[32:35], v[230:237], v[190:197], v[32:35]
	v_mfma_f32_16x16x128_f8f6f4 v[16:19], v[230:237], v[198:205], v[16:19]
	v_mfma_f32_16x16x128_f8f6f4 v[24:27], v[222:229], v[198:205], v[24:27]
	s_setprio 0
	s_barrier
	v_add_u32_e32 v220, s31, v147
	v_add_u32_e32 v221, s31, v148
	ds_read_b128 v[222:225], v220
	ds_read_b128 v[230:233], v220 offset:2048
	ds_read_b128 v[226:229], v221
	ds_read_b128 v[234:237], v221 offset:2048
	s_add_i32 s74, s74, s55
	v_lshl_add_u64 v[176:177], s[52:53], 0, v[136:137]
	s_mov_b32 m0, s74
	ds_read_b128 v[168:171], v150 offset:32768
	ds_read_b128 v[182:185], v150 offset:34816
	ds_read_b128 v[172:175], v151 offset:32768
	ds_read_b128 v[186:189], v151 offset:34816
	ds_read_b128 v[190:193], v150 offset:36864
	ds_read_b128 v[198:201], v150 offset:38912
	ds_read_b128 v[194:197], v151 offset:36864
	ds_read_b128 v[202:205], v151 offset:38912
	global_load_lds_dwordx4 v[176:177], off
	v_lshl_add_u64 v[176:177], s[52:53], 0, v[132:133]
	s_add_i32 m0, s74, 0x2000
	s_nop 0
	global_load_lds_dwordx4 v[176:177], off
	s_waitcnt vmcnt(6)
	s_waitcnt lgkmcnt(0)
	s_barrier
	s_setprio 1
	s_waitcnt lgkmcnt(0)
	v_mfma_f32_16x16x128_f8f6f4 v[128:131], v[222:229], v[168:175], v[128:131]
	v_mfma_f32_16x16x128_f8f6f4 v[124:127], v[230:237], v[168:175], v[124:127]
	v_mfma_f32_16x16x128_f8f6f4 v[112:115], v[230:237], v[182:189], v[112:115]
	v_mfma_f32_16x16x128_f8f6f4 v[120:123], v[222:229], v[182:189], v[120:123]
	v_mfma_f32_16x16x128_f8f6f4 v[104:107], v[222:229], v[190:197], v[104:107]
	v_mfma_f32_16x16x128_f8f6f4 v[96:99], v[230:237], v[190:197], v[96:99]
	v_mfma_f32_16x16x128_f8f6f4 v[80:83], v[230:237], v[198:205], v[80:83]
	v_mfma_f32_16x16x128_f8f6f4 v[88:91], v[222:229], v[198:205], v[88:91]
	s_setprio 0
	s_barrier
	s_add_i32 s74, 0, 0x1c000
	s_mov_b32 m0, s60
	v_add_u32_e32 v156, s74, v147
	v_add_u32_e32 v164, s74, v148
	v_lshl_add_u64 v[142:143], v[142:143], 0, s[20:21]
	ds_read_b128 v[152:155], v156
	ds_read_b128 v[160:163], v156 offset:2048
	ds_read_b128 v[156:159], v164
	ds_read_b128 v[164:167], v164 offset:2048
	global_load_lds_dwordx4 v[142:143], off
	v_lshl_add_u64 v[142:143], v[144:145], 0, s[20:21]
	s_mov_b32 m0, s61
	s_nop 0
	global_load_lds_dwordx4 v[142:143], off
	s_waitcnt vmcnt(6)
	s_waitcnt lgkmcnt(0)
	s_barrier
	s_setprio 1
	s_waitcnt lgkmcnt(0)
	v_mfma_f32_16x16x128_f8f6f4 v[116:119], v[152:159], v[168:175], v[116:119]
	v_mfma_f32_16x16x128_f8f6f4 v[108:111], v[160:167], v[168:175], v[108:111]
	v_mfma_f32_16x16x128_f8f6f4 v[92:95], v[160:167], v[182:189], v[92:95]
	v_mfma_f32_16x16x128_f8f6f4 v[100:103], v[152:159], v[182:189], v[100:103]
	v_mfma_f32_16x16x128_f8f6f4 v[84:87], v[152:159], v[190:197], v[84:87]
	v_mfma_f32_16x16x128_f8f6f4 v[76:79], v[160:167], v[190:197], v[76:79]
	v_mfma_f32_16x16x128_f8f6f4 v[68:71], v[160:167], v[198:205], v[68:71]
	v_mfma_f32_16x16x128_f8f6f4 v[72:75], v[152:159], v[198:205], v[72:75]
	s_setprio 0
	s_barrier
	s_add_u32 s52, s52, 0x40080
	s_addc_u32 s53, s53, 0
	s_add_i32 s74, s74, s55
	v_lshl_add_u64 v[142:143], s[52:53], 0, v[136:137]
	s_mov_b32 m0, s74
	ds_read_b128 v[168:171], v150 offset:49152
	ds_read_b128 v[182:185], v150 offset:51200
	ds_read_b128 v[172:175], v151 offset:49152
	ds_read_b128 v[186:189], v151 offset:51200
	ds_read_b128 v[190:193], v150 offset:53248
	ds_read_b128 v[198:201], v150 offset:55296
	ds_read_b128 v[194:197], v151 offset:53248
	ds_read_b128 v[202:205], v151 offset:55296
	global_load_lds_dwordx4 v[142:143], off
	v_lshl_add_u64 v[142:143], s[52:53], 0, v[132:133]
	s_add_i32 m0, s74, 0x2000
	s_nop 0
	global_load_lds_dwordx4 v[142:143], off
	s_waitcnt vmcnt(6)
	s_waitcnt lgkmcnt(0)
	s_barrier
	s_setprio 1
	s_waitcnt lgkmcnt(0)
	v_mfma_f32_16x16x128_f8f6f4 v[52:55], v[152:159], v[168:175], v[52:55]
	v_mfma_f32_16x16x128_f8f6f4 v[44:47], v[160:167], v[168:175], v[44:47]
	v_mfma_f32_16x16x128_f8f6f4 v[28:31], v[160:167], v[182:189], v[28:31]
	v_mfma_f32_16x16x128_f8f6f4 v[36:39], v[152:159], v[182:189], v[36:39]
	v_mfma_f32_16x16x128_f8f6f4 v[20:23], v[152:159], v[190:197], v[20:23]
	v_mfma_f32_16x16x128_f8f6f4 v[12:15], v[160:167], v[190:197], v[12:15]
	v_mfma_f32_16x16x128_f8f6f4 v[4:7], v[160:167], v[198:205], v[4:7]
	v_mfma_f32_16x16x128_f8f6f4 v[8:11], v[152:159], v[198:205], v[8:11]
	s_setprio 0
	s_barrier
	s_add_u32 s50, s50, 0x40080
	s_addc_u32 s51, s51, 0
	s_mov_b32 m0, s62
	v_lshl_add_u64 v[142:143], s[50:51], 0, v[2:3]
	global_load_lds_dwordx4 v[142:143], off
	v_lshl_add_u64 v[142:143], s[50:51], 0, v[134:135]
	s_mov_b32 m0, s63
	s_nop 0
	global_load_lds_dwordx4 v[142:143], off
	s_waitcnt vmcnt(6)
	s_waitcnt lgkmcnt(0)
	s_barrier
	s_setprio 1
	s_waitcnt lgkmcnt(0)
	v_mfma_f32_16x16x128_f8f6f4 v[64:67], v[222:229], v[168:175], v[64:67]
	v_mfma_f32_16x16x128_f8f6f4 v[60:63], v[230:237], v[168:175], v[60:63]
	v_mfma_f32_16x16x128_f8f6f4 v[48:51], v[230:237], v[182:189], v[48:51]
	v_mfma_f32_16x16x128_f8f6f4 v[56:59], v[222:229], v[182:189], v[56:59]
	v_mfma_f32_16x16x128_f8f6f4 v[40:43], v[222:229], v[190:197], v[40:43]
	v_mfma_f32_16x16x128_f8f6f4 v[32:35], v[230:237], v[190:197], v[32:35]
	v_mfma_f32_16x16x128_f8f6f4 v[16:19], v[230:237], v[198:205], v[16:19]
	v_mfma_f32_16x16x128_f8f6f4 v[24:27], v[222:229], v[198:205], v[24:27]
	s_setprio 0
	s_barrier
	s_add_i32 s73, s73, 2
	s_add_u32 s67, s67, 0x100
	s_addc_u32 s72, s72, 0
	s_add_u32 s48, s48, 0x100
	s_addc_u32 s49, s49, 0
	s_cmp_gt_u32 s73, 13
	s_cbranch_scc0 .LBB0_247
	v_lshl_or_b32 v144, s65, 8, v149
	v_lshl_add_u32 v156, s66, 8, v146
	v_ashrrev_i32_e32 v145, 31, v144
	v_mov_b64_e32 v[142:143], s[0:1]
	v_mad_i64_i32 v[152:153], s[8:9], v156, s94, v[142:143]
	v_lshlrev_b64 v[144:145], 1, v[144:145]
	v_pk_mul_f32 v[130:131], v[130:131], s[22:23] op_sel_hi:[1,0]
	v_pk_mul_f32 v[128:129], v[128:129], s[22:23] op_sel_hi:[1,0]
	v_pk_mul_f32 v[154:155], v[126:127], s[22:23] op_sel_hi:[1,0]
	v_pk_mul_f32 v[126:127], v[124:125], s[22:23] op_sel_hi:[1,0]
	v_lshl_add_u64 v[152:153], v[152:153], 0, v[144:145]
	v_cvt_pk_bf16_f32 v124, v128, v129
	v_cvt_pk_bf16_f32 v125, v130, v131
	v_cvt_pk_bf16_f32 v126, v126, v127
	v_cvt_pk_bf16_f32 v127, v154, v155
	global_store_dwordx4 v[152:153], v[124:127], off
	v_pk_mul_f32 v[118:119], v[118:119], s[22:23] op_sel_hi:[1,0]
	v_pk_mul_f32 v[116:117], v[116:117], s[22:23] op_sel_hi:[1,0]
	v_pk_mul_f32 v[124:125], v[110:111], s[22:23] op_sel_hi:[1,0]
	v_pk_mul_f32 v[110:111], v[108:109], s[22:23] op_sel_hi:[1,0]
	v_cvt_pk_bf16_f32 v108, v116, v117
	v_cvt_pk_bf16_f32 v109, v118, v119
	v_cvt_pk_bf16_f32 v110, v110, v111
	v_cvt_pk_bf16_f32 v111, v124, v125
	global_store_dwordx4 v[152:153], v[108:111], off offset:256
	v_pk_mul_f32 v[114:115], v[114:115], s[22:23] op_sel_hi:[1,0]
	v_pk_mul_f32 v[112:113], v[112:113], s[22:23] op_sel_hi:[1,0]
	v_or_b32_e32 v108, 16, v156
	v_mad_i64_i32 v[108:109], s[8:9], v108, s94, v[142:143]
	v_lshl_add_u64 v[116:117], v[108:109], 0, v[144:145]
	v_pk_mul_f32 v[110:111], v[122:123], s[22:23] op_sel_hi:[1,0]
	v_pk_mul_f32 v[108:109], v[120:121], s[22:23] op_sel_hi:[1,0]
	v_pk_mul_f32 v[102:103], v[102:103], s[22:23] op_sel_hi:[1,0]
	v_cvt_pk_bf16_f32 v108, v108, v109
	v_cvt_pk_bf16_f32 v109, v110, v111
	v_cvt_pk_bf16_f32 v110, v112, v113
	v_cvt_pk_bf16_f32 v111, v114, v115
	global_store_dwordx4 v[116:117], v[108:111], off
	v_pk_mul_f32 v[100:101], v[100:101], s[22:23] op_sel_hi:[1,0]
	v_pk_mul_f32 v[98:99], v[98:99], s[22:23] op_sel_hi:[1,0]
	v_pk_mul_f32 v[108:109], v[94:95], s[22:23] op_sel_hi:[1,0]
	v_pk_mul_f32 v[94:95], v[92:93], s[22:23] op_sel_hi:[1,0]
	v_cvt_pk_bf16_f32 v92, v100, v101
	v_cvt_pk_bf16_f32 v93, v102, v103
	v_cvt_pk_bf16_f32 v94, v94, v95
	v_cvt_pk_bf16_f32 v95, v108, v109
	global_store_dwordx4 v[116:117], v[92:95], off offset:256
	v_pk_mul_f32 v[96:97], v[96:97], s[22:23] op_sel_hi:[1,0]
	v_pk_mul_f32 v[86:87], v[86:87], s[22:23] op_sel_hi:[1,0]
	v_or_b32_e32 v92, 32, v156
	v_mad_i64_i32 v[92:93], s[8:9], v92, s94, v[142:143]
	v_lshl_add_u64 v[100:101], v[92:93], 0, v[144:145]
	v_pk_mul_f32 v[94:95], v[106:107], s[22:23] op_sel_hi:[1,0]
	v_pk_mul_f32 v[92:93], v[104:105], s[22:23] op_sel_hi:[1,0]
	v_pk_mul_f32 v[84:85], v[84:85], s[22:23] op_sel_hi:[1,0]
	v_cvt_pk_bf16_f32 v92, v92, v93
	v_cvt_pk_bf16_f32 v93, v94, v95
	v_cvt_pk_bf16_f32 v94, v96, v97
	v_cvt_pk_bf16_f32 v95, v98, v99
	global_store_dwordx4 v[100:101], v[92:95], off
	v_pk_mul_f32 v[82:83], v[82:83], s[22:23] op_sel_hi:[1,0]
	v_pk_mul_f32 v[80:81], v[80:81], s[22:23] op_sel_hi:[1,0]
	v_pk_mul_f32 v[92:93], v[78:79], s[22:23] op_sel_hi:[1,0]
	v_pk_mul_f32 v[78:79], v[76:77], s[22:23] op_sel_hi:[1,0]
	v_cvt_pk_bf16_f32 v76, v84, v85
	v_cvt_pk_bf16_f32 v77, v86, v87
	v_cvt_pk_bf16_f32 v78, v78, v79
	v_cvt_pk_bf16_f32 v79, v92, v93
	global_store_dwordx4 v[100:101], v[76:79], off offset:256
	v_pk_mul_f32 v[74:75], v[74:75], s[22:23] op_sel_hi:[1,0]
	v_pk_mul_f32 v[72:73], v[72:73], s[22:23] op_sel_hi:[1,0]
	v_or_b32_e32 v76, 48, v156
	v_mad_i64_i32 v[76:77], s[8:9], v76, s94, v[142:143]
	v_lshl_add_u64 v[84:85], v[76:77], 0, v[144:145]
	v_pk_mul_f32 v[78:79], v[90:91], s[22:23] op_sel_hi:[1,0]
	v_pk_mul_f32 v[76:77], v[88:89], s[22:23] op_sel_hi:[1,0]
	v_pk_mul_f32 v[66:67], v[66:67], s[22:23] op_sel_hi:[1,0]
	v_cvt_pk_bf16_f32 v76, v76, v77
	v_cvt_pk_bf16_f32 v77, v78, v79
	v_cvt_pk_bf16_f32 v78, v80, v81
	v_cvt_pk_bf16_f32 v79, v82, v83
	global_store_dwordx4 v[84:85], v[76:79], off
	v_pk_mul_f32 v[64:65], v[64:65], s[22:23] op_sel_hi:[1,0]
	v_pk_mul_f32 v[54:55], v[54:55], s[22:23] op_sel_hi:[1,0]
	v_pk_mul_f32 v[76:77], v[70:71], s[22:23] op_sel_hi:[1,0]
	v_pk_mul_f32 v[70:71], v[68:69], s[22:23] op_sel_hi:[1,0]
	v_cvt_pk_bf16_f32 v68, v72, v73
	v_cvt_pk_bf16_f32 v69, v74, v75
	v_cvt_pk_bf16_f32 v70, v70, v71
	v_cvt_pk_bf16_f32 v71, v76, v77
	global_store_dwordx4 v[84:85], v[68:71], off offset:256
	v_pk_mul_f32 v[52:53], v[52:53], s[22:23] op_sel_hi:[1,0]
	v_pk_mul_f32 v[50:51], v[50:51], s[22:23] op_sel_hi:[1,0]
	v_add_u32_e32 v68, 0x80, v156
	v_mad_i64_i32 v[68:69], s[8:9], v68, s94, v[142:143]
	v_pk_mul_f32 v[70:71], v[62:63], s[22:23] op_sel_hi:[1,0]
	v_pk_mul_f32 v[62:63], v[60:61], s[22:23] op_sel_hi:[1,0]
	v_lshl_add_u64 v[68:69], v[68:69], 0, v[144:145]
	v_cvt_pk_bf16_f32 v60, v64, v65
	v_cvt_pk_bf16_f32 v61, v66, v67
	v_cvt_pk_bf16_f32 v62, v62, v63
	v_cvt_pk_bf16_f32 v63, v70, v71
	global_store_dwordx4 v[68:69], v[60:63], off
	v_pk_mul_f32 v[48:49], v[48:49], s[22:23] op_sel_hi:[1,0]
	v_pk_mul_f32 v[38:39], v[38:39], s[22:23] op_sel_hi:[1,0]
	v_pk_mul_f32 v[60:61], v[46:47], s[22:23] op_sel_hi:[1,0]
	v_pk_mul_f32 v[46:47], v[44:45], s[22:23] op_sel_hi:[1,0]
	v_cvt_pk_bf16_f32 v44, v52, v53
	v_cvt_pk_bf16_f32 v45, v54, v55
	v_cvt_pk_bf16_f32 v46, v46, v47
	v_cvt_pk_bf16_f32 v47, v60, v61
	global_store_dwordx4 v[68:69], v[44:47], off offset:256
	v_pk_mul_f32 v[36:37], v[36:37], s[22:23] op_sel_hi:[1,0]
	v_pk_mul_f32 v[34:35], v[34:35], s[22:23] op_sel_hi:[1,0]
	v_add_u32_e32 v44, 0x90, v156
	v_mad_i64_i32 v[44:45], s[8:9], v44, s94, v[142:143]
	v_lshl_add_u64 v[52:53], v[44:45], 0, v[144:145]
	v_pk_mul_f32 v[46:47], v[58:59], s[22:23] op_sel_hi:[1,0]
	v_pk_mul_f32 v[44:45], v[56:57], s[22:23] op_sel_hi:[1,0]
	v_pk_mul_f32 v[32:33], v[32:33], s[22:23] op_sel_hi:[1,0]
	v_cvt_pk_bf16_f32 v44, v44, v45
	v_cvt_pk_bf16_f32 v45, v46, v47
	v_cvt_pk_bf16_f32 v46, v48, v49
	v_cvt_pk_bf16_f32 v47, v50, v51
	global_store_dwordx4 v[52:53], v[44:47], off
	v_pk_mul_f32 v[22:23], v[22:23], s[22:23] op_sel_hi:[1,0]
	v_pk_mul_f32 v[20:21], v[20:21], s[22:23] op_sel_hi:[1,0]
	v_pk_mul_f32 v[44:45], v[30:31], s[22:23] op_sel_hi:[1,0]
	v_pk_mul_f32 v[30:31], v[28:29], s[22:23] op_sel_hi:[1,0]
	v_cvt_pk_bf16_f32 v28, v36, v37
	v_cvt_pk_bf16_f32 v29, v38, v39
	v_cvt_pk_bf16_f32 v30, v30, v31
	v_cvt_pk_bf16_f32 v31, v44, v45
	global_store_dwordx4 v[52:53], v[28:31], off offset:256
	v_pk_mul_f32 v[18:19], v[18:19], s[22:23] op_sel_hi:[1,0]
	v_pk_mul_f32 v[16:17], v[16:17], s[22:23] op_sel_hi:[1,0]
	v_add_u32_e32 v28, 0xa0, v156
	v_mad_i64_i32 v[28:29], s[8:9], v28, s94, v[142:143]
	v_lshl_add_u64 v[36:37], v[28:29], 0, v[144:145]
	v_pk_mul_f32 v[30:31], v[42:43], s[22:23] op_sel_hi:[1,0]
	v_pk_mul_f32 v[28:29], v[40:41], s[22:23] op_sel_hi:[1,0]
	v_pk_mul_f32 v[10:11], v[10:11], s[22:23] op_sel_hi:[1,0]
	v_cvt_pk_bf16_f32 v28, v28, v29
	v_cvt_pk_bf16_f32 v29, v30, v31
	v_cvt_pk_bf16_f32 v30, v32, v33
	v_cvt_pk_bf16_f32 v31, v34, v35
	global_store_dwordx4 v[36:37], v[28:31], off
	v_pk_mul_f32 v[8:9], v[8:9], s[22:23] op_sel_hi:[1,0]
	s_and_b64 vcc, exec, s[40:41]
	v_pk_mul_f32 v[28:29], v[14:15], s[22:23] op_sel_hi:[1,0]
	v_pk_mul_f32 v[14:15], v[12:13], s[22:23] op_sel_hi:[1,0]
	v_cvt_pk_bf16_f32 v12, v20, v21
	v_cvt_pk_bf16_f32 v13, v22, v23
	v_cvt_pk_bf16_f32 v14, v14, v15
	v_cvt_pk_bf16_f32 v15, v28, v29
	global_store_dwordx4 v[36:37], v[12:15], off offset:256
	s_mov_b32 s65, s4
	s_mov_b32 s66, s42
	v_add_u32_e32 v12, 0xb0, v156
	v_mad_i64_i32 v[12:13], s[8:9], v12, s94, v[142:143]
	v_lshl_add_u64 v[20:21], v[12:13], 0, v[144:145]
	v_pk_mul_f32 v[14:15], v[26:27], s[22:23] op_sel_hi:[1,0]
	v_pk_mul_f32 v[12:13], v[24:25], s[22:23] op_sel_hi:[1,0]
	s_mov_b64 s[48:49], s[46:47]
	v_cvt_pk_bf16_f32 v12, v12, v13
	v_cvt_pk_bf16_f32 v13, v14, v15
	v_cvt_pk_bf16_f32 v14, v16, v17
	v_cvt_pk_bf16_f32 v15, v18, v19
	global_store_dwordx4 v[20:21], v[12:15], off
	s_mov_b64 s[50:51], s[44:45]
	s_nop 0
	v_pk_mul_f32 v[12:13], v[6:7], s[22:23] op_sel_hi:[1,0]
	v_pk_mul_f32 v[6:7], v[4:5], s[22:23] op_sel_hi:[1,0]
	v_cvt_pk_bf16_f32 v4, v8, v9
	v_cvt_pk_bf16_f32 v5, v10, v11
	v_cvt_pk_bf16_f32 v6, v6, v7
	v_cvt_pk_bf16_f32 v7, v12, v13
	global_store_dwordx4 v[20:21], v[4:7], off offset:256
	s_cbranch_vccz .LBB0_240
	s_waitcnt vmcnt(0)
	v_readlane_b32 s64, v253, 27
	v_readlane_b32 s66, v253, 29
	s_cmpk_gt_u32 s6, 0xff
	v_readlane_b32 s65, v253, 28
	v_readlane_b32 s67, v253, 30
	s_cbranch_scc1 .LBB0_251
	s_barrier

.LBB0_430:
	s_add_u32 s56, s54, 0x80
	s_addc_u32 s57, s55, 0
	s_add_i32 vcc_lo, 0, 0x10000
	v_add_u32_e32 v220, vcc_lo, v143
	v_add_u32_e32 v221, vcc_lo, v144
	ds_read_b128 v[222:225], v220
	ds_read_b128 v[230:233], v220 offset:2048
	ds_read_b128 v[226:229], v221
	ds_read_b128 v[234:237], v221 offset:2048
	s_cmp_eq_u32 s97, 12
	s_cselect_b32 s59, s5, s57
	s_cselect_b32 s58, s43, s56
	s_cselect_b32 s57, s8, s96
	s_cselect_b32 s56, s9, s89
	s_add_i32 s76, s31, s64
	v_lshl_add_u64 v[172:173], s[54:55], 0, v[140:141]
	s_mov_b32 m0, s76
	ds_read_b128 v[164:167], v146
	ds_read_b128 v[182:185], v146 offset:2048
	ds_read_b128 v[168:171], v147
	ds_read_b128 v[186:189], v147 offset:2048
	ds_read_b128 v[190:193], v146 offset:4096
	ds_read_b128 v[198:201], v146 offset:6144
	ds_read_b128 v[194:197], v147 offset:4096
	ds_read_b128 v[202:205], v147 offset:6144
	global_load_lds_dwordx4 v[172:173], off
	v_lshl_add_u64 v[172:173], s[54:55], 0, v[138:139]
	s_add_i32 m0, s76, 0x2000
	s_nop 0
	global_load_lds_dwordx4 v[172:173], off
	s_waitcnt vmcnt(6)
	s_waitcnt lgkmcnt(0)
	s_barrier
	s_setprio 1
	s_waitcnt lgkmcnt(0)
	v_mfma_f32_16x16x128_f8f6f4 v[128:131], v[222:229], v[164:171], v[128:131]
	v_mfma_f32_16x16x128_f8f6f4 v[124:127], v[230:237], v[164:171], v[124:127]
	v_mfma_f32_16x16x128_f8f6f4 v[108:111], v[230:237], v[182:189], v[108:111]
	v_mfma_f32_16x16x128_f8f6f4 v[116:119], v[222:229], v[182:189], v[116:119]
	v_mfma_f32_16x16x128_f8f6f4 v[100:103], v[222:229], v[190:197], v[100:103]
	v_mfma_f32_16x16x128_f8f6f4 v[92:95], v[230:237], v[190:197], v[92:95]
	v_mfma_f32_16x16x128_f8f6f4 v[76:79], v[230:237], v[198:205], v[76:79]
	v_mfma_f32_16x16x128_f8f6f4 v[84:87], v[222:229], v[198:205], v[84:87]
	s_setprio 0
	s_barrier
	s_add_i32 s76, 0, 0x14000
	s_mov_b32 m0, s45
	v_add_u32_e32 v152, s76, v143
	v_add_u32_e32 v160, s76, v144
	v_lshl_add_u64 v[172:173], s[56:57], 0, v[2:3]
	ds_read_b128 v[148:151], v152
	ds_read_b128 v[156:159], v152 offset:2048
	ds_read_b128 v[152:155], v160
	ds_read_b128 v[160:163], v160 offset:2048
	global_load_lds_dwordx4 v[172:173], off
	v_lshl_add_u64 v[174:175], s[56:57], 0, v[134:135]
	s_mov_b32 m0, s51
	s_nop 0
	global_load_lds_dwordx4 v[174:175], off
	s_waitcnt vmcnt(6)
	s_waitcnt lgkmcnt(0)
	s_barrier
	s_setprio 1
	s_waitcnt lgkmcnt(0)
	v_mfma_f32_16x16x128_f8f6f4 v[120:123], v[148:155], v[164:171], v[120:123]
	v_mfma_f32_16x16x128_f8f6f4 v[112:115], v[156:163], v[164:171], v[112:115]
	v_mfma_f32_16x16x128_f8f6f4 v[96:99], v[156:163], v[182:189], v[96:99]
	v_mfma_f32_16x16x128_f8f6f4 v[104:107], v[148:155], v[182:189], v[104:107]
	v_mfma_f32_16x16x128_f8f6f4 v[88:91], v[148:155], v[190:197], v[88:91]
	v_mfma_f32_16x16x128_f8f6f4 v[80:83], v[156:163], v[190:197], v[80:83]
	v_mfma_f32_16x16x128_f8f6f4 v[68:71], v[156:163], v[198:205], v[68:71]
	v_mfma_f32_16x16x128_f8f6f4 v[72:75], v[148:155], v[198:205], v[72:75]
	s_setprio 0
	s_barrier
	s_add_u32 s80, s58, 0x40000
	s_addc_u32 s81, s59, 0
	s_add_i32 s76, s76, s64
	v_lshl_add_u64 v[176:177], s[80:81], 0, v[136:137]
	s_mov_b32 m0, s76
	ds_read_b128 v[164:167], v146 offset:16384
	ds_read_b128 v[182:185], v146 offset:18432
	ds_read_b128 v[168:171], v147 offset:16384
	ds_read_b128 v[186:189], v147 offset:18432
	ds_read_b128 v[190:193], v146 offset:20480
	ds_read_b128 v[198:201], v146 offset:22528
	ds_read_b128 v[194:197], v147 offset:20480
	ds_read_b128 v[202:205], v147 offset:22528
	global_load_lds_dwordx4 v[176:177], off
	v_lshl_add_u64 v[176:177], s[80:81], 0, v[132:133]
	s_add_i32 m0, s76, 0x2000
	s_nop 0
	global_load_lds_dwordx4 v[176:177], off
	s_waitcnt vmcnt(6)
	s_waitcnt lgkmcnt(0)
	s_barrier
	s_setprio 1
	s_waitcnt lgkmcnt(0)
	v_mfma_f32_16x16x128_f8f6f4 v[56:59], v[148:155], v[164:171], v[56:59]
	v_mfma_f32_16x16x128_f8f6f4 v[48:51], v[156:163], v[164:171], v[48:51]
	v_mfma_f32_16x16x128_f8f6f4 v[32:35], v[156:163], v[182:189], v[32:35]
	v_mfma_f32_16x16x128_f8f6f4 v[40:43], v[148:155], v[182:189], v[40:43]
	v_mfma_f32_16x16x128_f8f6f4 v[24:27], v[148:155], v[190:197], v[24:27]
	v_mfma_f32_16x16x128_f8f6f4 v[16:19], v[156:163], v[190:197], v[16:19]
	v_mfma_f32_16x16x128_f8f6f4 v[4:7], v[156:163], v[198:205], v[4:7]
	v_mfma_f32_16x16x128_f8f6f4 v[8:11], v[148:155], v[198:205], v[8:11]
	s_setprio 0
	s_barrier
	s_add_u32 s80, s56, 0x40000
	s_addc_u32 s81, s57, 0
	s_mov_b32 m0, s66
	v_lshl_add_u64 v[176:177], s[80:81], 0, v[2:3]
	global_load_lds_dwordx4 v[176:177], off
	v_lshl_add_u64 v[176:177], s[80:81], 0, v[134:135]
	s_mov_b32 m0, s67
	s_nop 0
	global_load_lds_dwordx4 v[176:177], off
	s_waitcnt vmcnt(6)
	s_waitcnt lgkmcnt(0)
	s_barrier
	s_setprio 1
	s_waitcnt lgkmcnt(0)
	v_mfma_f32_16x16x128_f8f6f4 v[64:67], v[222:229], v[164:171], v[64:67]
	v_mfma_f32_16x16x128_f8f6f4 v[60:63], v[230:237], v[164:171], v[60:63]
	v_mfma_f32_16x16x128_f8f6f4 v[44:47], v[230:237], v[182:189], v[44:47]
	v_mfma_f32_16x16x128_f8f6f4 v[52:55], v[222:229], v[182:189], v[52:55]
	v_mfma_f32_16x16x128_f8f6f4 v[36:39], v[222:229], v[190:197], v[36:39]
	v_mfma_f32_16x16x128_f8f6f4 v[28:31], v[230:237], v[190:197], v[28:31]
	v_mfma_f32_16x16x128_f8f6f4 v[12:15], v[230:237], v[198:205], v[12:15]
	v_mfma_f32_16x16x128_f8f6f4 v[20:23], v[222:229], v[198:205], v[20:23]
	s_setprio 0
	s_barrier
	v_add_u32_e32 v220, s31, v143
	v_add_u32_e32 v221, s31, v144
	ds_read_b128 v[222:225], v220
	ds_read_b128 v[230:233], v220 offset:2048
	ds_read_b128 v[226:229], v221
	ds_read_b128 v[234:237], v221 offset:2048
	s_add_i32 s76, vcc_lo, s64
	v_lshl_add_u64 v[176:177], s[58:59], 0, v[136:137]
	s_mov_b32 m0, s76
	ds_read_b128 v[164:167], v146 offset:32768
	ds_read_b128 v[182:185], v146 offset:34816
	ds_read_b128 v[168:171], v147 offset:32768
	ds_read_b128 v[186:189], v147 offset:34816
	ds_read_b128 v[190:193], v146 offset:36864
	ds_read_b128 v[198:201], v146 offset:38912
	ds_read_b128 v[194:197], v147 offset:36864
	ds_read_b128 v[202:205], v147 offset:38912
	global_load_lds_dwordx4 v[176:177], off
	v_lshl_add_u64 v[176:177], s[58:59], 0, v[132:133]
	s_add_i32 m0, s76, 0x2000
	s_nop 0
	global_load_lds_dwordx4 v[176:177], off
	s_waitcnt vmcnt(6)
	s_waitcnt lgkmcnt(0)
	s_barrier
	s_setprio 1
	s_waitcnt lgkmcnt(0)
	v_mfma_f32_16x16x128_f8f6f4 v[128:131], v[222:229], v[164:171], v[128:131]
	v_mfma_f32_16x16x128_f8f6f4 v[124:127], v[230:237], v[164:171], v[124:127]
	v_mfma_f32_16x16x128_f8f6f4 v[108:111], v[230:237], v[182:189], v[108:111]
	v_mfma_f32_16x16x128_f8f6f4 v[116:119], v[222:229], v[182:189], v[116:119]
	v_mfma_f32_16x16x128_f8f6f4 v[100:103], v[222:229], v[190:197], v[100:103]
	v_mfma_f32_16x16x128_f8f6f4 v[92:95], v[230:237], v[190:197], v[92:95]
	v_mfma_f32_16x16x128_f8f6f4 v[76:79], v[230:237], v[198:205], v[76:79]
	v_mfma_f32_16x16x128_f8f6f4 v[84:87], v[222:229], v[198:205], v[84:87]
	s_setprio 0
	s_barrier
	s_add_i32 s76, 0, 0x1c000
	s_mov_b32 m0, s72
	v_add_u32_e32 v152, s76, v143
	v_add_u32_e32 v160, s76, v144
	v_lshl_add_u64 v[172:173], v[172:173], 0, s[20:21]
	ds_read_b128 v[148:151], v152
	ds_read_b128 v[156:159], v152 offset:2048
	ds_read_b128 v[152:155], v160
	ds_read_b128 v[160:163], v160 offset:2048
	global_load_lds_dwordx4 v[172:173], off
	v_lshl_add_u64 v[172:173], v[174:175], 0, s[20:21]
	s_mov_b32 m0, s73
	s_nop 0
	global_load_lds_dwordx4 v[172:173], off
	s_waitcnt vmcnt(6)
	s_waitcnt lgkmcnt(0)
	s_barrier
	s_setprio 1
	s_waitcnt lgkmcnt(0)
	v_mfma_f32_16x16x128_f8f6f4 v[120:123], v[148:155], v[164:171], v[120:123]
	v_mfma_f32_16x16x128_f8f6f4 v[112:115], v[156:163], v[164:171], v[112:115]
	v_mfma_f32_16x16x128_f8f6f4 v[96:99], v[156:163], v[182:189], v[96:99]
	v_mfma_f32_16x16x128_f8f6f4 v[104:107], v[148:155], v[182:189], v[104:107]
	v_mfma_f32_16x16x128_f8f6f4 v[88:91], v[148:155], v[190:197], v[88:91]
	v_mfma_f32_16x16x128_f8f6f4 v[80:83], v[156:163], v[190:197], v[80:83]
	v_mfma_f32_16x16x128_f8f6f4 v[68:71], v[156:163], v[198:205], v[68:71]
	v_mfma_f32_16x16x128_f8f6f4 v[72:75], v[148:155], v[198:205], v[72:75]
	s_setprio 0
	s_barrier
	s_add_u32 s58, s58, 0x40080
	s_addc_u32 s59, s59, 0
	s_add_i32 s76, s76, s64
	v_lshl_add_u64 v[172:173], s[58:59], 0, v[136:137]
	s_mov_b32 m0, s76
	ds_read_b128 v[164:167], v146 offset:49152
	ds_read_b128 v[182:185], v146 offset:51200
	ds_read_b128 v[168:171], v147 offset:49152
	ds_read_b128 v[186:189], v147 offset:51200
	ds_read_b128 v[190:193], v146 offset:53248
	ds_read_b128 v[198:201], v146 offset:55296
	ds_read_b128 v[194:197], v147 offset:53248
	ds_read_b128 v[202:205], v147 offset:55296
	global_load_lds_dwordx4 v[172:173], off
	v_lshl_add_u64 v[172:173], s[58:59], 0, v[132:133]
	s_add_i32 m0, s76, 0x2000
	s_nop 0
	global_load_lds_dwordx4 v[172:173], off
	s_waitcnt vmcnt(6)
	s_waitcnt lgkmcnt(0)
	s_barrier
	s_setprio 1
	s_waitcnt lgkmcnt(0)
	v_mfma_f32_16x16x128_f8f6f4 v[56:59], v[148:155], v[164:171], v[56:59]
	v_mfma_f32_16x16x128_f8f6f4 v[48:51], v[156:163], v[164:171], v[48:51]
	v_mfma_f32_16x16x128_f8f6f4 v[32:35], v[156:163], v[182:189], v[32:35]
	v_mfma_f32_16x16x128_f8f6f4 v[40:43], v[148:155], v[182:189], v[40:43]
	v_mfma_f32_16x16x128_f8f6f4 v[24:27], v[148:155], v[190:197], v[24:27]
	v_mfma_f32_16x16x128_f8f6f4 v[16:19], v[156:163], v[190:197], v[16:19]
	v_mfma_f32_16x16x128_f8f6f4 v[4:7], v[156:163], v[198:205], v[4:7]
	v_mfma_f32_16x16x128_f8f6f4 v[8:11], v[148:155], v[198:205], v[8:11]
	s_setprio 0
	s_barrier
	s_add_u32 s56, s56, 0x40080
	s_addc_u32 s57, s57, 0
	s_mov_b32 m0, s74
	v_lshl_add_u64 v[172:173], s[56:57], 0, v[2:3]
	global_load_lds_dwordx4 v[172:173], off
	v_lshl_add_u64 v[172:173], s[56:57], 0, v[134:135]
	s_mov_b32 m0, s75
	s_nop 0
	global_load_lds_dwordx4 v[172:173], off
	s_waitcnt vmcnt(6)
	s_waitcnt lgkmcnt(0)
	s_barrier
	s_setprio 1
	s_waitcnt lgkmcnt(0)
	v_mfma_f32_16x16x128_f8f6f4 v[64:67], v[222:229], v[164:171], v[64:67]
	v_mfma_f32_16x16x128_f8f6f4 v[60:63], v[230:237], v[164:171], v[60:63]
	v_mfma_f32_16x16x128_f8f6f4 v[44:47], v[230:237], v[182:189], v[44:47]
	v_mfma_f32_16x16x128_f8f6f4 v[52:55], v[222:229], v[182:189], v[52:55]
	v_mfma_f32_16x16x128_f8f6f4 v[36:39], v[222:229], v[190:197], v[36:39]
	v_mfma_f32_16x16x128_f8f6f4 v[28:31], v[230:237], v[190:197], v[28:31]
	v_mfma_f32_16x16x128_f8f6f4 v[12:15], v[230:237], v[198:205], v[12:15]
	v_mfma_f32_16x16x128_f8f6f4 v[20:23], v[222:229], v[198:205], v[20:23]
	s_setprio 0
	s_barrier
	s_add_i32 s97, s97, 2
	s_add_u32 s89, s89, 0x100
	s_addc_u32 s96, s96, 0
	s_add_u32 s54, s54, 0x100
	s_addc_u32 s55, s55, 0
	s_cmp_gt_u32 s97, 13
	s_cbranch_scc0 .LBB0_430
	v_mul_f32_e32 v152, 0x3c000000, v128
	v_mul_f32_e32 v129, 0x3c000000, v129
	v_mov_b32_e32 v128, v3
	v_cvt_pk_fp8_f32 v128, v152, v129
	v_mul_f32_e32 v124, 0x3c000000, v124
	v_mul_f32_e32 v125, 0x3c000000, v125
	v_mov_b32_e32 v129, v3
	v_cvt_pk_fp8_f32 v129, v124, v125
	v_mul_f32_e32 v124, 0x3c000000, v126
	v_mul_f32_e32 v125, 0x3c000000, v127
	v_mul_f32_e32 v121, 0x3c000000, v121
	v_cvt_pk_fp8_f32 v129, v124, v125 op_sel:[0,0,1]
	v_mul_f32_e32 v124, 0x3c000000, v120
	v_mov_b32_e32 v120, v3
	v_cvt_pk_fp8_f32 v120, v124, v121
	v_mul_f32_e32 v112, 0x3c000000, v112
	v_mul_f32_e32 v113, 0x3c000000, v113
	v_mov_b32_e32 v121, v3
	v_cvt_pk_fp8_f32 v121, v112, v113
	v_mul_f32_e32 v130, 0x3c000000, v130
	v_mul_f32_e32 v131, 0x3c000000, v131
	v_lshl_add_u32 v148, s50, 8, v142
	v_lshl_or_b32 v150, s44, 8, v145
	v_cvt_pk_fp8_f32 v128, v130, v131 op_sel:[0,0,1]
	v_mul_f32_e32 v122, 0x3c000000, v122
	v_mul_f32_e32 v123, 0x3c000000, v123
	v_mul_f32_e32 v112, 0x3c000000, v114
	v_mul_f32_e32 v113, 0x3c000000, v115
	v_ashrrev_i32_e32 v151, 31, v150
	v_ashrrev_i32_e32 v149, 31, v148
	v_cvt_pk_fp8_f32 v120, v122, v123 op_sel:[0,0,1]
	v_cvt_pk_fp8_f32 v121, v112, v113 op_sel:[0,0,1]
	v_lshl_add_u64 v[150:151], s[0:1], 0, v[150:151]
	v_lshlrev_b64 v[112:113], 11, v[148:149]
	v_lshl_add_u64 v[112:113], v[150:151], 0, v[112:113]
	global_store_dwordx2 v[112:113], v[128:129], off
	global_store_dwordx2 v[112:113], v[120:121], off offset:128
	v_mul_f32_e32 v120, 0x3c000000, v116
	v_mul_f32_e32 v117, 0x3c000000, v117
	v_mov_b32_e32 v116, v3
	v_cvt_pk_fp8_f32 v116, v120, v117
	v_mul_f32_e32 v108, 0x3c000000, v108
	v_mul_f32_e32 v109, 0x3c000000, v109
	v_mov_b32_e32 v117, v3
	v_cvt_pk_fp8_f32 v117, v108, v109
	v_mul_f32_e32 v108, 0x3c000000, v110
	v_mul_f32_e32 v109, 0x3c000000, v111
	v_mul_f32_e32 v105, 0x3c000000, v105
	v_cvt_pk_fp8_f32 v117, v108, v109 op_sel:[0,0,1]
	v_mul_f32_e32 v108, 0x3c000000, v104
	v_mov_b32_e32 v104, v3
	v_cvt_pk_fp8_f32 v104, v108, v105
	v_mul_f32_e32 v96, 0x3c000000, v96
	v_mul_f32_e32 v97, 0x3c000000, v97
	v_mov_b32_e32 v105, v3
	v_cvt_pk_fp8_f32 v105, v96, v97
	v_mul_f32_e32 v96, 0x3c000000, v98
	v_mul_f32_e32 v97, 0x3c000000, v99
	v_mul_f32_e32 v99, 0x3c000000, v100
	v_mul_f32_e32 v100, 0x3c000000, v101
	v_mov_b32_e32 v98, v3
	v_cvt_pk_fp8_f32 v98, v99, v100
	v_mul_f32_e32 v92, 0x3c000000, v92
	v_mul_f32_e32 v93, 0x3c000000, v93
	v_mov_b32_e32 v99, v3
	v_cvt_pk_fp8_f32 v99, v92, v93
	v_mul_f32_e32 v92, 0x3c000000, v94
	v_mul_f32_e32 v93, 0x3c000000, v95
	v_mul_f32_e32 v89, 0x3c000000, v89
	v_cvt_pk_fp8_f32 v99, v92, v93 op_sel:[0,0,1]
	v_mul_f32_e32 v92, 0x3c000000, v88
	v_mov_b32_e32 v88, v3
	v_cvt_pk_fp8_f32 v88, v92, v89
	v_mul_f32_e32 v80, 0x3c000000, v80
	v_mul_f32_e32 v81, 0x3c000000, v81
	v_mov_b32_e32 v89, v3
	v_cvt_pk_fp8_f32 v89, v80, v81
	v_mul_f32_e32 v80, 0x3c000000, v82
	v_mul_f32_e32 v81, 0x3c000000, v83
	v_mul_f32_e32 v83, 0x3c000000, v84
	v_mul_f32_e32 v84, 0x3c000000, v85
	v_mov_b32_e32 v82, v3
	v_cvt_pk_fp8_f32 v82, v83, v84
	v_mul_f32_e32 v76, 0x3c000000, v76
	v_mul_f32_e32 v77, 0x3c000000, v77
	v_mov_b32_e32 v83, v3
	v_cvt_pk_fp8_f32 v83, v76, v77
	v_mul_f32_e32 v76, 0x3c000000, v78
	v_mul_f32_e32 v77, 0x3c000000, v79
	v_mul_f32_e32 v73, 0x3c000000, v73
	v_cvt_pk_fp8_f32 v83, v76, v77 op_sel:[0,0,1]
	v_mul_f32_e32 v76, 0x3c000000, v72
	v_mov_b32_e32 v72, v3
	v_cvt_pk_fp8_f32 v72, v76, v73
	v_mul_f32_e32 v68, 0x3c000000, v68
	v_mul_f32_e32 v69, 0x3c000000, v69
	v_mov_b32_e32 v73, v3
	v_cvt_pk_fp8_f32 v73, v68, v69
	v_mul_f32_e32 v68, 0x3c000000, v70
	v_mul_f32_e32 v70, 0x3c000000, v64
	v_mul_f32_e32 v65, 0x3c000000, v65
	v_mov_b32_e32 v64, v3
	v_cvt_pk_fp8_f32 v64, v70, v65
	v_mul_f32_e32 v60, 0x3c000000, v60
	v_mul_f32_e32 v61, 0x3c000000, v61
	v_mov_b32_e32 v65, v3
	v_cvt_pk_fp8_f32 v65, v60, v61
	v_mul_f32_e32 v60, 0x3c000000, v62
	v_mul_f32_e32 v61, 0x3c000000, v63
	v_mul_f32_e32 v57, 0x3c000000, v57
	v_cvt_pk_fp8_f32 v65, v60, v61 op_sel:[0,0,1]
	v_mul_f32_e32 v60, 0x3c000000, v56
	v_mov_b32_e32 v56, v3
	v_cvt_pk_fp8_f32 v56, v60, v57
	v_mul_f32_e32 v48, 0x3c000000, v48
	v_mul_f32_e32 v49, 0x3c000000, v49
	v_mov_b32_e32 v57, v3
	v_cvt_pk_fp8_f32 v57, v48, v49
	v_mul_f32_e32 v48, 0x3c000000, v50
	v_mul_f32_e32 v49, 0x3c000000, v51
	v_mul_f32_e32 v51, 0x3c000000, v52
	v_mul_f32_e32 v52, 0x3c000000, v53
	v_mov_b32_e32 v50, v3
	v_cvt_pk_fp8_f32 v50, v51, v52
	v_mul_f32_e32 v44, 0x3c000000, v44
	v_mul_f32_e32 v45, 0x3c000000, v45
	v_mov_b32_e32 v51, v3
	v_cvt_pk_fp8_f32 v51, v44, v45
	v_mul_f32_e32 v44, 0x3c000000, v46
	v_mul_f32_e32 v45, 0x3c000000, v47
	v_mul_f32_e32 v41, 0x3c000000, v41
	v_cvt_pk_fp8_f32 v51, v44, v45 op_sel:[0,0,1]
	v_mul_f32_e32 v44, 0x3c000000, v40
	v_mov_b32_e32 v40, v3
	v_cvt_pk_fp8_f32 v40, v44, v41
	v_mul_f32_e32 v32, 0x3c000000, v32
	v_mul_f32_e32 v33, 0x3c000000, v33
	v_mov_b32_e32 v41, v3
	v_cvt_pk_fp8_f32 v41, v32, v33
	v_mul_f32_e32 v32, 0x3c000000, v34
	v_mul_f32_e32 v33, 0x3c000000, v35
	v_mul_f32_e32 v35, 0x3c000000, v36
	v_mul_f32_e32 v36, 0x3c000000, v37
	v_mov_b32_e32 v34, v3
	v_cvt_pk_fp8_f32 v34, v35, v36
	v_mul_f32_e32 v28, 0x3c000000, v28
	v_mul_f32_e32 v29, 0x3c000000, v29
	v_mov_b32_e32 v35, v3
	v_cvt_pk_fp8_f32 v35, v28, v29
	v_mul_f32_e32 v28, 0x3c000000, v30
	v_mul_f32_e32 v29, 0x3c000000, v31
	v_mul_f32_e32 v25, 0x3c000000, v25
	v_cvt_pk_fp8_f32 v35, v28, v29 op_sel:[0,0,1]
	v_mul_f32_e32 v28, 0x3c000000, v24
	v_mov_b32_e32 v24, v3
	v_mul_f32_e32 v118, 0x3c000000, v118
	v_mul_f32_e32 v119, 0x3c000000, v119
	v_cvt_pk_fp8_f32 v24, v28, v25
	v_mul_f32_e32 v16, 0x3c000000, v16
	v_mul_f32_e32 v17, 0x3c000000, v17
	v_mov_b32_e32 v25, v3
	v_or_b32_e32 v114, 16, v148
	v_cvt_pk_fp8_f32 v116, v118, v119 op_sel:[0,0,1]
	v_mul_f32_e32 v106, 0x3c000000, v106
	v_mul_f32_e32 v107, 0x3c000000, v107
	v_cvt_pk_fp8_f32 v25, v16, v17
	v_mul_f32_e32 v16, 0x3c000000, v18
	v_mul_f32_e32 v17, 0x3c000000, v19
	v_mul_f32_e32 v19, 0x3c000000, v20
	v_mul_f32_e32 v20, 0x3c000000, v21
	v_mov_b32_e32 v18, v3
	v_ashrrev_i32_e32 v115, 31, v114
	v_cvt_pk_fp8_f32 v104, v106, v107 op_sel:[0,0,1]
	v_cvt_pk_fp8_f32 v105, v96, v97 op_sel:[0,0,1]
	v_cvt_pk_fp8_f32 v18, v19, v20
	v_mul_f32_e32 v12, 0x3c000000, v12
	v_mul_f32_e32 v13, 0x3c000000, v13
	v_mov_b32_e32 v19, v3
	v_lshlrev_b64 v[96:97], 11, v[114:115]
	v_cvt_pk_fp8_f32 v19, v12, v13
	v_lshl_add_u64 v[96:97], v[150:151], 0, v[96:97]
	v_mul_f32_e32 v100, 0x3c000000, v102
	v_mul_f32_e32 v101, 0x3c000000, v103
	global_store_dwordx2 v[96:97], v[116:117], off
	global_store_dwordx2 v[96:97], v[104:105], off offset:128
	v_or_b32_e32 v96, 32, v148
	v_cvt_pk_fp8_f32 v98, v100, v101 op_sel:[0,0,1]
	v_mul_f32_e32 v90, 0x3c000000, v90
	v_mul_f32_e32 v91, 0x3c000000, v91
	v_ashrrev_i32_e32 v97, 31, v96
	v_cvt_pk_fp8_f32 v88, v90, v91 op_sel:[0,0,1]
	v_cvt_pk_fp8_f32 v89, v80, v81 op_sel:[0,0,1]
	s_mov_b32 s5, 0x40000
	v_mul_f32_e32 v12, 0x3c000000, v14
	v_mul_f32_e32 v13, 0x3c000000, v15
	v_lshlrev_b64 v[80:81], 11, v[96:97]
	v_cvt_pk_fp8_f32 v57, v48, v49 op_sel:[0,0,1]
	v_add_co_u32_e32 v48, vcc, s5, v112
	v_cvt_pk_fp8_f32 v19, v12, v13 op_sel:[0,0,1]
	v_mul_f32_e32 v12, 0x3c000000, v8
	v_mul_f32_e32 v9, 0x3c000000, v9
	v_mov_b32_e32 v8, v3
	v_lshl_add_u64 v[80:81], v[150:151], 0, v[80:81]
	v_mul_f32_e32 v84, 0x3c000000, v86
	v_mul_f32_e32 v85, 0x3c000000, v87
	v_addc_co_u32_e32 v49, vcc, 0, v113, vcc
	s_mov_b32 s5, 0x48000
	v_cvt_pk_fp8_f32 v8, v12, v9
	v_mul_f32_e32 v4, 0x3c000000, v4
	v_mul_f32_e32 v5, 0x3c000000, v5
	v_mov_b32_e32 v9, v3
	global_store_dwordx2 v[80:81], v[98:99], off
	global_store_dwordx2 v[80:81], v[88:89], off offset:128
	v_or_b32_e32 v80, 48, v148
	v_cvt_pk_fp8_f32 v82, v84, v85 op_sel:[0,0,1]
	v_mul_f32_e32 v74, 0x3c000000, v74
	v_mul_f32_e32 v75, 0x3c000000, v75
	v_mul_f32_e32 v69, 0x3c000000, v71
	v_mul_f32_e32 v66, 0x3c000000, v66
	v_mul_f32_e32 v67, 0x3c000000, v67
	v_cvt_pk_fp8_f32 v41, v32, v33 op_sel:[0,0,1]
	v_add_co_u32_e32 v32, vcc, s5, v112
	v_cvt_pk_fp8_f32 v9, v4, v5
	v_ashrrev_i32_e32 v81, 31, v80
	v_cvt_pk_fp8_f32 v72, v74, v75 op_sel:[0,0,1]
	v_cvt_pk_fp8_f32 v73, v68, v69 op_sel:[0,0,1]
	v_cvt_pk_fp8_f32 v64, v66, v67 op_sel:[0,0,1]
	v_mul_f32_e32 v58, 0x3c000000, v58
	v_mul_f32_e32 v59, 0x3c000000, v59
	v_mul_f32_e32 v52, 0x3c000000, v54
	v_mul_f32_e32 v53, 0x3c000000, v55
	v_addc_co_u32_e32 v33, vcc, 0, v113, vcc
	s_mov_b32 s5, 0x50000
	v_lshlrev_b64 v[68:69], 11, v[80:81]
	v_cvt_pk_fp8_f32 v56, v58, v59 op_sel:[0,0,1]
	v_cvt_pk_fp8_f32 v50, v52, v53 op_sel:[0,0,1]
	v_mul_f32_e32 v42, 0x3c000000, v42
	v_mul_f32_e32 v43, 0x3c000000, v43
	v_mul_f32_e32 v36, 0x3c000000, v38
	v_mul_f32_e32 v37, 0x3c000000, v39
	v_cvt_pk_fp8_f32 v25, v16, v17 op_sel:[0,0,1]
	v_add_co_u32_e32 v16, vcc, s5, v112
	v_mul_f32_e32 v20, 0x3c000000, v22
	v_mul_f32_e32 v21, 0x3c000000, v23
	v_lshl_add_u64 v[68:69], v[150:151], 0, v[68:69]
	s_mov_b64 s[8:9], 0x40000
	v_cvt_pk_fp8_f32 v40, v42, v43 op_sel:[0,0,1]
	v_cvt_pk_fp8_f32 v34, v36, v37 op_sel:[0,0,1]
	v_mul_f32_e32 v26, 0x3c000000, v26
	v_mul_f32_e32 v27, 0x3c000000, v27
	v_addc_co_u32_e32 v17, vcc, 0, v113, vcc
	v_cvt_pk_fp8_f32 v18, v20, v21 op_sel:[0,0,1]
	v_mul_f32_e32 v10, 0x3c000000, v10
	v_mul_f32_e32 v11, 0x3c000000, v11
	v_mul_f32_e32 v4, 0x3c000000, v6
	v_mul_f32_e32 v5, 0x3c000000, v7
	s_mov_b32 s5, 0x58000
	global_store_dwordx2 v[68:69], v[82:83], off
	global_store_dwordx2 v[68:69], v[72:73], off offset:128
	v_lshl_add_u64 v[68:69], v[112:113], 0, s[8:9]
	s_mov_b64 s[8:9], 0x48000
	v_cvt_pk_fp8_f32 v24, v26, v27 op_sel:[0,0,1]
	v_cvt_pk_fp8_f32 v8, v10, v11 op_sel:[0,0,1]
	v_cvt_pk_fp8_f32 v9, v4, v5 op_sel:[0,0,1]
	v_add_co_u32_e32 v4, vcc, s5, v112
	global_store_dwordx2 v[48:49], v[64:65], off
	global_store_dwordx2 v[68:69], v[56:57], off offset:128
	v_lshl_add_u64 v[48:49], v[112:113], 0, s[8:9]
	s_mov_b64 s[8:9], 0x50000
	v_addc_co_u32_e32 v5, vcc, 0, v113, vcc
	global_store_dwordx2 v[32:33], v[50:51], off
	global_store_dwordx2 v[48:49], v[40:41], off offset:128
	v_lshl_add_u64 v[32:33], v[112:113], 0, s[8:9]
	s_mov_b64 s[8:9], 0x58000
	s_and_b64 vcc, exec, s[40:41]
	s_mov_b32 s44, s4
	s_mov_b32 s50, s42
	s_mov_b64 s[54:55], s[52:53]
	s_mov_b64 s[56:57], s[46:47]
	global_store_dwordx2 v[16:17], v[34:35], off
	global_store_dwordx2 v[32:33], v[24:25], off offset:128
	v_lshl_add_u64 v[16:17], v[112:113], 0, s[8:9]
	global_store_dwordx2 v[4:5], v[18:19], off
	global_store_dwordx2 v[16:17], v[8:9], off offset:128
	s_cbranch_vccz .LBB0_427
	s_waitcnt vmcnt(0)
	v_readlane_b32 s86, v253, 23
	v_readlane_b32 s88, v253, 25
	s_cmpk_gt_u32 s27, 0xff
	v_readlane_b32 s84, v253, 20
	v_readlane_b32 s76, v253, 22
	v_readlane_b32 s87, v253, 24
	v_readlane_b32 s89, v253, 26
	v_readlane_b32 s85, v253, 21
	s_cbranch_scc1 .LBB0_434
	s_barrier

.LBB0_605:
	s_add_u32 s56, s54, 0x80
	s_addc_u32 s57, s55, 0
	s_add_i32 vcc_lo, 0, 0x10000
	v_add_u32_e32 v220, vcc_lo, v145
	v_add_u32_e32 v221, vcc_lo, v146
	ds_read_b128 v[222:225], v220
	ds_read_b128 v[230:233], v220 offset:2048
	ds_read_b128 v[226:229], v221
	ds_read_b128 v[234:237], v221 offset:2048
	s_cmp_eq_u32 s97, 12
	s_cselect_b32 s59, s45, s57
	s_cselect_b32 s58, s47, s56
	s_cselect_b32 s57, s8, s96
	s_cselect_b32 s56, s9, s89
	s_add_i32 s76, s31, s64
	v_lshl_add_u64 v[142:143], s[54:55], 0, v[140:141]
	s_mov_b32 m0, s76
	ds_read_b128 v[166:169], v148
	ds_read_b128 v[182:185], v148 offset:2048
	ds_read_b128 v[170:173], v149
	ds_read_b128 v[186:189], v149 offset:2048
	ds_read_b128 v[190:193], v148 offset:4096
	ds_read_b128 v[198:201], v148 offset:6144
	ds_read_b128 v[194:197], v149 offset:4096
	ds_read_b128 v[202:205], v149 offset:6144
	global_load_lds_dwordx4 v[142:143], off
	v_lshl_add_u64 v[142:143], s[54:55], 0, v[138:139]
	s_add_i32 m0, s76, 0x2000
	s_nop 0
	global_load_lds_dwordx4 v[142:143], off
	s_waitcnt vmcnt(6)
	s_waitcnt lgkmcnt(0)
	s_barrier
	s_setprio 1
	s_waitcnt lgkmcnt(0)
	v_mfma_f32_16x16x128_f8f6f4 v[128:131], v[222:229], v[166:173], v[128:131]
	v_mfma_f32_16x16x128_f8f6f4 v[124:127], v[230:237], v[166:173], v[124:127]
	v_mfma_f32_16x16x128_f8f6f4 v[112:115], v[230:237], v[182:189], v[112:115]
	v_mfma_f32_16x16x128_f8f6f4 v[120:123], v[222:229], v[182:189], v[120:123]
	v_mfma_f32_16x16x128_f8f6f4 v[104:107], v[222:229], v[190:197], v[104:107]
	v_mfma_f32_16x16x128_f8f6f4 v[96:99], v[230:237], v[190:197], v[96:99]
	v_mfma_f32_16x16x128_f8f6f4 v[80:83], v[230:237], v[198:205], v[80:83]
	v_mfma_f32_16x16x128_f8f6f4 v[88:91], v[222:229], v[198:205], v[88:91]
	s_setprio 0
	s_barrier
	s_add_i32 s76, 0, 0x14000
	v_add_u32_e32 v142, s76, v145
	v_add_u32_e32 v143, s76, v146
	s_mov_b32 m0, s5
	ds_read_b128 v[150:153], v142
	ds_read_b128 v[158:161], v142 offset:2048
	ds_read_b128 v[154:157], v143
	ds_read_b128 v[162:165], v143 offset:2048
	v_lshl_add_u64 v[142:143], s[56:57], 0, v[2:3]
	global_load_lds_dwordx4 v[142:143], off
	v_lshl_add_u64 v[174:175], s[56:57], 0, v[134:135]
	s_mov_b32 m0, s43
	s_nop 0
	global_load_lds_dwordx4 v[174:175], off
	s_waitcnt vmcnt(6)
	s_waitcnt lgkmcnt(0)
	s_barrier
	s_setprio 1
	s_waitcnt lgkmcnt(0)
	v_mfma_f32_16x16x128_f8f6f4 v[116:119], v[150:157], v[166:173], v[116:119]
	v_mfma_f32_16x16x128_f8f6f4 v[108:111], v[158:165], v[166:173], v[108:111]
	v_mfma_f32_16x16x128_f8f6f4 v[92:95], v[158:165], v[182:189], v[92:95]
	v_mfma_f32_16x16x128_f8f6f4 v[100:103], v[150:157], v[182:189], v[100:103]
	v_mfma_f32_16x16x128_f8f6f4 v[84:87], v[150:157], v[190:197], v[84:87]
	v_mfma_f32_16x16x128_f8f6f4 v[76:79], v[158:165], v[190:197], v[76:79]
	v_mfma_f32_16x16x128_f8f6f4 v[68:71], v[158:165], v[198:205], v[68:71]
	v_mfma_f32_16x16x128_f8f6f4 v[72:75], v[150:157], v[198:205], v[72:75]
	s_setprio 0
	s_barrier
	s_add_u32 s80, s58, 0x40000
	s_addc_u32 s81, s59, 0
	s_add_i32 s76, s76, s64
	v_lshl_add_u64 v[176:177], s[80:81], 0, v[136:137]
	s_mov_b32 m0, s76
	ds_read_b128 v[166:169], v148 offset:16384
	ds_read_b128 v[182:185], v148 offset:18432
	ds_read_b128 v[170:173], v149 offset:16384
	ds_read_b128 v[186:189], v149 offset:18432
	ds_read_b128 v[190:193], v148 offset:20480
	ds_read_b128 v[198:201], v148 offset:22528
	ds_read_b128 v[194:197], v149 offset:20480
	ds_read_b128 v[202:205], v149 offset:22528
	global_load_lds_dwordx4 v[176:177], off
	v_lshl_add_u64 v[176:177], s[80:81], 0, v[132:133]
	s_add_i32 m0, s76, 0x2000
	s_nop 0
	global_load_lds_dwordx4 v[176:177], off
	s_waitcnt vmcnt(6)
	s_waitcnt lgkmcnt(0)
	s_barrier
	s_setprio 1
	s_waitcnt lgkmcnt(0)
	v_mfma_f32_16x16x128_f8f6f4 v[52:55], v[150:157], v[166:173], v[52:55]
	v_mfma_f32_16x16x128_f8f6f4 v[44:47], v[158:165], v[166:173], v[44:47]
	v_mfma_f32_16x16x128_f8f6f4 v[28:31], v[158:165], v[182:189], v[28:31]
	v_mfma_f32_16x16x128_f8f6f4 v[36:39], v[150:157], v[182:189], v[36:39]
	v_mfma_f32_16x16x128_f8f6f4 v[20:23], v[150:157], v[190:197], v[20:23]
	v_mfma_f32_16x16x128_f8f6f4 v[12:15], v[158:165], v[190:197], v[12:15]
	v_mfma_f32_16x16x128_f8f6f4 v[4:7], v[158:165], v[198:205], v[4:7]
	v_mfma_f32_16x16x128_f8f6f4 v[8:11], v[150:157], v[198:205], v[8:11]
	s_setprio 0
	s_barrier
	s_add_u32 s80, s56, 0x40000
	s_addc_u32 s81, s57, 0
	s_mov_b32 m0, s66
	v_lshl_add_u64 v[176:177], s[80:81], 0, v[2:3]
	global_load_lds_dwordx4 v[176:177], off
	v_lshl_add_u64 v[176:177], s[80:81], 0, v[134:135]
	s_mov_b32 m0, s67
	s_nop 0
	global_load_lds_dwordx4 v[176:177], off
	s_waitcnt vmcnt(6)
	s_waitcnt lgkmcnt(0)
	s_barrier
	s_setprio 1
	s_waitcnt lgkmcnt(0)
	v_mfma_f32_16x16x128_f8f6f4 v[64:67], v[222:229], v[166:173], v[64:67]
	v_mfma_f32_16x16x128_f8f6f4 v[60:63], v[230:237], v[166:173], v[60:63]
	v_mfma_f32_16x16x128_f8f6f4 v[48:51], v[230:237], v[182:189], v[48:51]
	v_mfma_f32_16x16x128_f8f6f4 v[56:59], v[222:229], v[182:189], v[56:59]
	v_mfma_f32_16x16x128_f8f6f4 v[40:43], v[222:229], v[190:197], v[40:43]
	v_mfma_f32_16x16x128_f8f6f4 v[32:35], v[230:237], v[190:197], v[32:35]
	v_mfma_f32_16x16x128_f8f6f4 v[16:19], v[230:237], v[198:205], v[16:19]
	v_mfma_f32_16x16x128_f8f6f4 v[24:27], v[222:229], v[198:205], v[24:27]
	s_setprio 0
	s_barrier
	v_add_u32_e32 v220, s31, v145
	v_add_u32_e32 v221, s31, v146
	ds_read_b128 v[222:225], v220
	ds_read_b128 v[230:233], v220 offset:2048
	ds_read_b128 v[226:229], v221
	ds_read_b128 v[234:237], v221 offset:2048
	s_add_i32 s76, vcc_lo, s64
	v_lshl_add_u64 v[176:177], s[58:59], 0, v[136:137]
	s_mov_b32 m0, s76
	ds_read_b128 v[166:169], v148 offset:32768
	ds_read_b128 v[182:185], v148 offset:34816
	ds_read_b128 v[170:173], v149 offset:32768
	ds_read_b128 v[186:189], v149 offset:34816
	ds_read_b128 v[190:193], v148 offset:36864
	ds_read_b128 v[198:201], v148 offset:38912
	ds_read_b128 v[194:197], v149 offset:36864
	ds_read_b128 v[202:205], v149 offset:38912
	global_load_lds_dwordx4 v[176:177], off
	v_lshl_add_u64 v[176:177], s[58:59], 0, v[132:133]
	s_add_i32 m0, s76, 0x2000
	s_nop 0
	global_load_lds_dwordx4 v[176:177], off
	s_waitcnt vmcnt(6)
	s_waitcnt lgkmcnt(0)
	s_barrier
	s_setprio 1
	s_waitcnt lgkmcnt(0)
	v_mfma_f32_16x16x128_f8f6f4 v[128:131], v[222:229], v[166:173], v[128:131]
	v_mfma_f32_16x16x128_f8f6f4 v[124:127], v[230:237], v[166:173], v[124:127]
	v_mfma_f32_16x16x128_f8f6f4 v[112:115], v[230:237], v[182:189], v[112:115]
	v_mfma_f32_16x16x128_f8f6f4 v[120:123], v[222:229], v[182:189], v[120:123]
	v_mfma_f32_16x16x128_f8f6f4 v[104:107], v[222:229], v[190:197], v[104:107]
	v_mfma_f32_16x16x128_f8f6f4 v[96:99], v[230:237], v[190:197], v[96:99]
	v_mfma_f32_16x16x128_f8f6f4 v[80:83], v[230:237], v[198:205], v[80:83]
	v_mfma_f32_16x16x128_f8f6f4 v[88:91], v[222:229], v[198:205], v[88:91]
	s_setprio 0
	s_barrier
	s_add_i32 s76, 0, 0x1c000
	s_mov_b32 m0, s72
	v_add_u32_e32 v154, s76, v145
	v_add_u32_e32 v162, s76, v146
	v_lshl_add_u64 v[142:143], v[142:143], 0, s[20:21]
	ds_read_b128 v[150:153], v154
	ds_read_b128 v[158:161], v154 offset:2048
	ds_read_b128 v[154:157], v162
	ds_read_b128 v[162:165], v162 offset:2048
	global_load_lds_dwordx4 v[142:143], off
	v_lshl_add_u64 v[142:143], v[174:175], 0, s[20:21]
	s_mov_b32 m0, s73
	s_nop 0
	global_load_lds_dwordx4 v[142:143], off
	s_waitcnt vmcnt(6)
	s_waitcnt lgkmcnt(0)
	s_barrier
	s_setprio 1
	s_waitcnt lgkmcnt(0)
	v_mfma_f32_16x16x128_f8f6f4 v[116:119], v[150:157], v[166:173], v[116:119]
	v_mfma_f32_16x16x128_f8f6f4 v[108:111], v[158:165], v[166:173], v[108:111]
	v_mfma_f32_16x16x128_f8f6f4 v[92:95], v[158:165], v[182:189], v[92:95]
	v_mfma_f32_16x16x128_f8f6f4 v[100:103], v[150:157], v[182:189], v[100:103]
	v_mfma_f32_16x16x128_f8f6f4 v[84:87], v[150:157], v[190:197], v[84:87]
	v_mfma_f32_16x16x128_f8f6f4 v[76:79], v[158:165], v[190:197], v[76:79]
	v_mfma_f32_16x16x128_f8f6f4 v[68:71], v[158:165], v[198:205], v[68:71]
	v_mfma_f32_16x16x128_f8f6f4 v[72:75], v[150:157], v[198:205], v[72:75]
	s_setprio 0
	s_barrier
	s_add_u32 s58, s58, 0x40080
	s_addc_u32 s59, s59, 0
	s_add_i32 s76, s76, s64
	v_lshl_add_u64 v[142:143], s[58:59], 0, v[136:137]
	s_mov_b32 m0, s76
	ds_read_b128 v[166:169], v148 offset:49152
	ds_read_b128 v[182:185], v148 offset:51200
	ds_read_b128 v[170:173], v149 offset:49152
	ds_read_b128 v[186:189], v149 offset:51200
	ds_read_b128 v[190:193], v148 offset:53248
	ds_read_b128 v[198:201], v148 offset:55296
	ds_read_b128 v[194:197], v149 offset:53248
	ds_read_b128 v[202:205], v149 offset:55296
	global_load_lds_dwordx4 v[142:143], off
	v_lshl_add_u64 v[142:143], s[58:59], 0, v[132:133]
	s_add_i32 m0, s76, 0x2000
	s_nop 0
	global_load_lds_dwordx4 v[142:143], off
	s_waitcnt vmcnt(6)
	s_waitcnt lgkmcnt(0)
	s_barrier
	s_setprio 1
	s_waitcnt lgkmcnt(0)
	v_mfma_f32_16x16x128_f8f6f4 v[52:55], v[150:157], v[166:173], v[52:55]
	v_mfma_f32_16x16x128_f8f6f4 v[44:47], v[158:165], v[166:173], v[44:47]
	v_mfma_f32_16x16x128_f8f6f4 v[28:31], v[158:165], v[182:189], v[28:31]
	v_mfma_f32_16x16x128_f8f6f4 v[36:39], v[150:157], v[182:189], v[36:39]
	v_mfma_f32_16x16x128_f8f6f4 v[20:23], v[150:157], v[190:197], v[20:23]
	v_mfma_f32_16x16x128_f8f6f4 v[12:15], v[158:165], v[190:197], v[12:15]
	v_mfma_f32_16x16x128_f8f6f4 v[4:7], v[158:165], v[198:205], v[4:7]
	v_mfma_f32_16x16x128_f8f6f4 v[8:11], v[150:157], v[198:205], v[8:11]
	s_setprio 0
	s_barrier
	s_add_u32 s56, s56, 0x40080
	s_addc_u32 s57, s57, 0
	s_mov_b32 m0, s74
	v_lshl_add_u64 v[142:143], s[56:57], 0, v[2:3]
	global_load_lds_dwordx4 v[142:143], off
	v_lshl_add_u64 v[142:143], s[56:57], 0, v[134:135]
	s_mov_b32 m0, s75
	s_nop 0
	global_load_lds_dwordx4 v[142:143], off
	s_waitcnt vmcnt(6)
	s_waitcnt lgkmcnt(0)
	s_barrier
	s_setprio 1
	s_waitcnt lgkmcnt(0)
	v_mfma_f32_16x16x128_f8f6f4 v[64:67], v[222:229], v[166:173], v[64:67]
	v_mfma_f32_16x16x128_f8f6f4 v[60:63], v[230:237], v[166:173], v[60:63]
	v_mfma_f32_16x16x128_f8f6f4 v[48:51], v[230:237], v[182:189], v[48:51]
	v_mfma_f32_16x16x128_f8f6f4 v[56:59], v[222:229], v[182:189], v[56:59]
	v_mfma_f32_16x16x128_f8f6f4 v[40:43], v[222:229], v[190:197], v[40:43]
	v_mfma_f32_16x16x128_f8f6f4 v[32:35], v[230:237], v[190:197], v[32:35]
	v_mfma_f32_16x16x128_f8f6f4 v[16:19], v[230:237], v[198:205], v[16:19]
	v_mfma_f32_16x16x128_f8f6f4 v[24:27], v[222:229], v[198:205], v[24:27]
	s_setprio 0
	s_barrier
	s_add_i32 s97, s97, 2
	s_add_u32 s89, s89, 0x100
	s_addc_u32 s96, s96, 0
	s_add_u32 s54, s54, 0x100
	s_addc_u32 s55, s55, 0
	s_cmp_gt_u32 s97, 13
	s_cbranch_scc0 .LBB0_605
	v_lshl_add_u32 v150, s42, 8, v144
	v_lshl_or_b32 v142, s4, 8, v147
	v_ashrrev_i32_e32 v151, 31, v150
	v_ashrrev_i32_e32 v143, 31, v142
	v_lshlrev_b64 v[152:153], 12, v[150:151]
	v_lshl_add_u64 v[152:153], s[0:1], 0, v[152:153]
	v_lshlrev_b64 v[154:155], 1, v[142:143]
	v_lshl_add_u64 v[142:143], v[152:153], 0, v[154:155]
	v_pk_mul_f32 v[130:131], v[130:131], s[22:23] op_sel_hi:[1,0]
	v_pk_mul_f32 v[128:129], v[128:129], s[22:23] op_sel_hi:[1,0]
	v_pk_mul_f32 v[152:153], v[126:127], s[22:23] op_sel_hi:[1,0]
	v_pk_mul_f32 v[126:127], v[124:125], s[22:23] op_sel_hi:[1,0]
	v_cvt_pk_bf16_f32 v124, v128, v129
	v_cvt_pk_bf16_f32 v125, v130, v131
	v_cvt_pk_bf16_f32 v126, v126, v127
	v_cvt_pk_bf16_f32 v127, v152, v153
	global_store_dwordx4 v[142:143], v[124:127], off
	v_pk_mul_f32 v[118:119], v[118:119], s[22:23] op_sel_hi:[1,0]
	v_pk_mul_f32 v[116:117], v[116:117], s[22:23] op_sel_hi:[1,0]
	v_pk_mul_f32 v[124:125], v[110:111], s[22:23] op_sel_hi:[1,0]
	v_pk_mul_f32 v[110:111], v[108:109], s[22:23] op_sel_hi:[1,0]
	v_cvt_pk_bf16_f32 v108, v116, v117
	v_cvt_pk_bf16_f32 v109, v118, v119
	v_cvt_pk_bf16_f32 v110, v110, v111
	v_cvt_pk_bf16_f32 v111, v124, v125
	global_store_dwordx4 v[142:143], v[108:111], off offset:256
	v_pk_mul_f32 v[114:115], v[114:115], s[22:23] op_sel_hi:[1,0]
	v_pk_mul_f32 v[112:113], v[112:113], s[22:23] op_sel_hi:[1,0]
	v_or_b32_e32 v108, 16, v150
	v_ashrrev_i32_e32 v109, 31, v108
	v_lshlrev_b64 v[108:109], 12, v[108:109]
	v_lshl_add_u64 v[108:109], s[0:1], 0, v[108:109]
	v_lshl_add_u64 v[116:117], v[108:109], 0, v[154:155]
	v_pk_mul_f32 v[110:111], v[122:123], s[22:23] op_sel_hi:[1,0]
	v_pk_mul_f32 v[108:109], v[120:121], s[22:23] op_sel_hi:[1,0]
	v_pk_mul_f32 v[102:103], v[102:103], s[22:23] op_sel_hi:[1,0]
	v_cvt_pk_bf16_f32 v108, v108, v109
	v_cvt_pk_bf16_f32 v109, v110, v111
	v_cvt_pk_bf16_f32 v110, v112, v113
	v_cvt_pk_bf16_f32 v111, v114, v115
	global_store_dwordx4 v[116:117], v[108:111], off
	v_pk_mul_f32 v[100:101], v[100:101], s[22:23] op_sel_hi:[1,0]
	v_pk_mul_f32 v[98:99], v[98:99], s[22:23] op_sel_hi:[1,0]
	v_pk_mul_f32 v[108:109], v[94:95], s[22:23] op_sel_hi:[1,0]
	v_pk_mul_f32 v[94:95], v[92:93], s[22:23] op_sel_hi:[1,0]
	v_cvt_pk_bf16_f32 v92, v100, v101
	v_cvt_pk_bf16_f32 v93, v102, v103
	v_cvt_pk_bf16_f32 v94, v94, v95
	v_cvt_pk_bf16_f32 v95, v108, v109
	global_store_dwordx4 v[116:117], v[92:95], off offset:256
	v_pk_mul_f32 v[96:97], v[96:97], s[22:23] op_sel_hi:[1,0]
	v_pk_mul_f32 v[86:87], v[86:87], s[22:23] op_sel_hi:[1,0]
	v_or_b32_e32 v92, 32, v150
	v_ashrrev_i32_e32 v93, 31, v92
	v_lshlrev_b64 v[92:93], 12, v[92:93]
	v_lshl_add_u64 v[92:93], s[0:1], 0, v[92:93]
	v_lshl_add_u64 v[100:101], v[92:93], 0, v[154:155]
	v_pk_mul_f32 v[94:95], v[106:107], s[22:23] op_sel_hi:[1,0]
	v_pk_mul_f32 v[92:93], v[104:105], s[22:23] op_sel_hi:[1,0]
	v_pk_mul_f32 v[84:85], v[84:85], s[22:23] op_sel_hi:[1,0]
	v_cvt_pk_bf16_f32 v92, v92, v93
	v_cvt_pk_bf16_f32 v93, v94, v95
	v_cvt_pk_bf16_f32 v94, v96, v97
	v_cvt_pk_bf16_f32 v95, v98, v99
	global_store_dwordx4 v[100:101], v[92:95], off
	v_pk_mul_f32 v[82:83], v[82:83], s[22:23] op_sel_hi:[1,0]
	v_pk_mul_f32 v[80:81], v[80:81], s[22:23] op_sel_hi:[1,0]
	v_pk_mul_f32 v[92:93], v[78:79], s[22:23] op_sel_hi:[1,0]
	v_pk_mul_f32 v[78:79], v[76:77], s[22:23] op_sel_hi:[1,0]
	v_cvt_pk_bf16_f32 v76, v84, v85
	v_cvt_pk_bf16_f32 v77, v86, v87
	v_cvt_pk_bf16_f32 v78, v78, v79
	v_cvt_pk_bf16_f32 v79, v92, v93
	global_store_dwordx4 v[100:101], v[76:79], off offset:256
	v_pk_mul_f32 v[74:75], v[74:75], s[22:23] op_sel_hi:[1,0]
	v_pk_mul_f32 v[72:73], v[72:73], s[22:23] op_sel_hi:[1,0]
	v_or_b32_e32 v76, 48, v150
	v_ashrrev_i32_e32 v77, 31, v76
	v_lshlrev_b64 v[76:77], 12, v[76:77]
	v_lshl_add_u64 v[76:77], s[0:1], 0, v[76:77]
	v_lshl_add_u64 v[84:85], v[76:77], 0, v[154:155]
	v_pk_mul_f32 v[78:79], v[90:91], s[22:23] op_sel_hi:[1,0]
	v_pk_mul_f32 v[76:77], v[88:89], s[22:23] op_sel_hi:[1,0]
	v_pk_mul_f32 v[64:65], v[64:65], s[22:23] op_sel_hi:[1,0]
	v_cvt_pk_bf16_f32 v76, v76, v77
	v_cvt_pk_bf16_f32 v77, v78, v79
	v_cvt_pk_bf16_f32 v78, v80, v81
	v_cvt_pk_bf16_f32 v79, v82, v83
	global_store_dwordx4 v[84:85], v[76:79], off
	s_mov_b32 s4, 0x80000
	v_pk_mul_f32 v[66:67], v[66:67], s[22:23] op_sel_hi:[1,0]
	v_pk_mul_f32 v[76:77], v[70:71], s[22:23] op_sel_hi:[1,0]
	v_pk_mul_f32 v[70:71], v[68:69], s[22:23] op_sel_hi:[1,0]
	v_cvt_pk_bf16_f32 v68, v72, v73
	v_cvt_pk_bf16_f32 v69, v74, v75
	v_cvt_pk_bf16_f32 v70, v70, v71
	v_cvt_pk_bf16_f32 v71, v76, v77
	global_store_dwordx4 v[84:85], v[68:71], off offset:256
	s_mov_b64 s[8:9], 0x80000
	v_pk_mul_f32 v[54:55], v[54:55], s[22:23] op_sel_hi:[1,0]
	v_pk_mul_f32 v[70:71], v[62:63], s[22:23] op_sel_hi:[1,0]
	v_pk_mul_f32 v[62:63], v[60:61], s[22:23] op_sel_hi:[1,0]
	v_cvt_pk_bf16_f32 v60, v64, v65
	v_add_co_u32_e32 v64, vcc, s4, v142
	v_cvt_pk_bf16_f32 v61, v66, v67
	v_cvt_pk_bf16_f32 v62, v62, v63
	v_cvt_pk_bf16_f32 v63, v70, v71
	v_addc_co_u32_e32 v65, vcc, 0, v143, vcc
	global_store_dwordx4 v[64:65], v[60:63], off
	v_pk_mul_f32 v[52:53], v[52:53], s[22:23] op_sel_hi:[1,0]
	v_lshl_add_u64 v[68:69], v[142:143], 0, s[8:9]
	v_pk_mul_f32 v[60:61], v[46:47], s[22:23] op_sel_hi:[1,0]
	v_pk_mul_f32 v[46:47], v[44:45], s[22:23] op_sel_hi:[1,0]
	v_cvt_pk_bf16_f32 v44, v52, v53
	v_cvt_pk_bf16_f32 v45, v54, v55
	v_cvt_pk_bf16_f32 v46, v46, v47
	v_cvt_pk_bf16_f32 v47, v60, v61
	global_store_dwordx4 v[68:69], v[44:47], off offset:256
	v_pk_mul_f32 v[48:49], v[48:49], s[22:23] op_sel_hi:[1,0]
	s_mov_b32 s4, 0x90000
	v_pk_mul_f32 v[46:47], v[58:59], s[22:23] op_sel_hi:[1,0]
	v_pk_mul_f32 v[44:45], v[56:57], s[22:23] op_sel_hi:[1,0]
	v_pk_mul_f32 v[50:51], v[50:51], s[22:23] op_sel_hi:[1,0]
	v_cvt_pk_bf16_f32 v44, v44, v45
	v_cvt_pk_bf16_f32 v45, v46, v47
	v_cvt_pk_bf16_f32 v46, v48, v49
	v_add_co_u32_e32 v48, vcc, s4, v142
	v_cvt_pk_bf16_f32 v47, v50, v51
	s_nop 0
	v_addc_co_u32_e32 v49, vcc, 0, v143, vcc
	s_mov_b64 s[8:9], 0x90000
	global_store_dwordx4 v[48:49], v[44:47], off
	v_pk_mul_f32 v[38:39], v[38:39], s[22:23] op_sel_hi:[1,0]
	v_pk_mul_f32 v[36:37], v[36:37], s[22:23] op_sel_hi:[1,0]
	v_pk_mul_f32 v[44:45], v[30:31], s[22:23] op_sel_hi:[1,0]
	v_pk_mul_f32 v[30:31], v[28:29], s[22:23] op_sel_hi:[1,0]
	v_lshl_add_u64 v[52:53], v[142:143], 0, s[8:9]
	v_cvt_pk_bf16_f32 v28, v36, v37
	v_cvt_pk_bf16_f32 v29, v38, v39
	v_cvt_pk_bf16_f32 v30, v30, v31
	v_cvt_pk_bf16_f32 v31, v44, v45
	global_store_dwordx4 v[52:53], v[28:31], off offset:256
	v_pk_mul_f32 v[32:33], v[32:33], s[22:23] op_sel_hi:[1,0]
	s_mov_b32 s4, 0xa0000
	v_pk_mul_f32 v[30:31], v[42:43], s[22:23] op_sel_hi:[1,0]
	v_pk_mul_f32 v[28:29], v[40:41], s[22:23] op_sel_hi:[1,0]
	v_pk_mul_f32 v[34:35], v[34:35], s[22:23] op_sel_hi:[1,0]
	v_cvt_pk_bf16_f32 v28, v28, v29
	v_cvt_pk_bf16_f32 v29, v30, v31
	v_cvt_pk_bf16_f32 v30, v32, v33
	v_add_co_u32_e32 v32, vcc, s4, v142
	v_cvt_pk_bf16_f32 v31, v34, v35
	s_nop 0
	v_addc_co_u32_e32 v33, vcc, 0, v143, vcc
	s_mov_b64 s[8:9], 0xa0000
	global_store_dwordx4 v[32:33], v[28:31], off
	v_pk_mul_f32 v[22:23], v[22:23], s[22:23] op_sel_hi:[1,0]
	v_pk_mul_f32 v[20:21], v[20:21], s[22:23] op_sel_hi:[1,0]
	v_pk_mul_f32 v[28:29], v[14:15], s[22:23] op_sel_hi:[1,0]
	v_pk_mul_f32 v[14:15], v[12:13], s[22:23] op_sel_hi:[1,0]
	v_lshl_add_u64 v[36:37], v[142:143], 0, s[8:9]
	v_cvt_pk_bf16_f32 v12, v20, v21
	v_cvt_pk_bf16_f32 v13, v22, v23
	v_cvt_pk_bf16_f32 v14, v14, v15
	v_cvt_pk_bf16_f32 v15, v28, v29
	global_store_dwordx4 v[36:37], v[12:15], off offset:256
	v_pk_mul_f32 v[16:17], v[16:17], s[22:23] op_sel_hi:[1,0]
	s_mov_b32 s4, 0xb0000
	v_pk_mul_f32 v[14:15], v[26:27], s[22:23] op_sel_hi:[1,0]
	v_pk_mul_f32 v[12:13], v[24:25], s[22:23] op_sel_hi:[1,0]
	v_pk_mul_f32 v[18:19], v[18:19], s[22:23] op_sel_hi:[1,0]
	v_cvt_pk_bf16_f32 v12, v12, v13
	v_cvt_pk_bf16_f32 v13, v14, v15
	v_cvt_pk_bf16_f32 v14, v16, v17
	v_add_co_u32_e32 v16, vcc, s4, v142
	v_cvt_pk_bf16_f32 v15, v18, v19
	s_nop 0
	v_addc_co_u32_e32 v17, vcc, 0, v143, vcc
	s_mov_b64 s[8:9], 0xb0000
	global_store_dwordx4 v[16:17], v[12:15], off
	v_pk_mul_f32 v[10:11], v[10:11], s[22:23] op_sel_hi:[1,0]
	v_pk_mul_f32 v[8:9], v[8:9], s[22:23] op_sel_hi:[1,0]
	v_pk_mul_f32 v[12:13], v[6:7], s[22:23] op_sel_hi:[1,0]
	v_pk_mul_f32 v[6:7], v[4:5], s[22:23] op_sel_hi:[1,0]
	v_lshl_add_u64 v[20:21], v[142:143], 0, s[8:9]
	v_cvt_pk_bf16_f32 v4, v8, v9
	v_cvt_pk_bf16_f32 v5, v10, v11
	v_cvt_pk_bf16_f32 v6, v6, v7
	v_cvt_pk_bf16_f32 v7, v12, v13
	s_and_b64 vcc, exec, s[40:41]
	s_mov_b32 s4, s44
	s_mov_b32 s42, s46
	s_mov_b64 s[54:55], s[52:53]
	s_mov_b64 s[56:57], s[50:51]
	global_store_dwordx4 v[20:21], v[4:7], off offset:256
	s_cbranch_vccz .LBB0_602
	s_waitcnt vmcnt(0)
	v_readlane_b32 s86, v253, 23
	v_readlane_b32 s88, v253, 25
	s_cmpk_gt_u32 s27, 0xff
	v_readlane_b32 s84, v253, 20
	v_readlane_b32 s76, v253, 22
	v_readlane_b32 s87, v253, 24
	v_readlane_b32 s89, v253, 26
	v_readlane_b32 s85, v253, 21
	s_cbranch_scc1 .LBB0_609
	s_barrier
